# nt (streaming) policy on read-once loads: hg_scan U, P1 x rows, P6 residual x, one P0 GEMV load
# speedup vs baseline: 1.0116x; 1.0116x over previous
.LBB0_20:
	v_lshl_add_u64 v[20:21], v[12:13], 0, s[8:9]
	v_add_co_u32_e32 v22, vcc, s11, v20
	global_load_dwordx4 v[16:19], v[20:21], off nt
	s_nop 0
	v_addc_co_u32_e32 v23, vcc, 0, v21, vcc
	v_add_co_u32_e32 v24, vcc, s12, v20
	v_mov_b32_e32 v60, s7
	s_nop 0
	v_addc_co_u32_e32 v25, vcc, 0, v21, vcc
	v_add_co_u32_e32 v28, vcc, s13, v20
	s_add_u32 s8, s8, 0x60000
	s_nop 0
	v_addc_co_u32_e32 v29, vcc, 0, v21, vcc
	v_add_co_u32_e32 v32, vcc, s14, v20
	s_addc_u32 s9, s9, 0
	s_nop 0
	v_addc_co_u32_e32 v33, vcc, 0, v21, vcc
	v_add_co_u32_e32 v36, vcc, s15, v20
	s_add_i32 s7, s7, 32
	s_nop 0
	v_addc_co_u32_e32 v37, vcc, 0, v21, vcc
	v_add_co_u32_e32 v40, vcc, s16, v20
	s_cmp_eq_u32 s8, 0x180000
	s_nop 0
	v_addc_co_u32_e32 v41, vcc, 0, v21, vcc
	v_add_co_u32_e32 v44, vcc, s17, v20
	s_nop 1
	v_addc_co_u32_e32 v45, vcc, 0, v21, vcc
	global_load_dwordx4 v[20:23], v[22:23], off
	s_nop 0
	global_load_dwordx4 v[24:27], v[24:25], off
	s_nop 0
	global_load_dwordx4 v[28:31], v[28:29], off
	s_nop 0
	global_load_dwordx4 v[32:35], v[32:33], off
	s_nop 0
	global_load_dwordx4 v[36:39], v[36:37], off
	s_nop 0
	global_load_dwordx4 v[40:43], v[40:41], off
	s_nop 0
	global_load_dwordx4 v[44:47], v[44:45], off
	ds_read_b128 v[48:51], v60
	ds_read_b128 v[52:55], v60 offset:16
	ds_read_b128 v[56:59], v60 offset:8192
	ds_read_b128 v[60:63], v60 offset:8208
	s_waitcnt lgkmcnt(3)
	v_mov_b32_e32 v64, v51
	s_waitcnt lgkmcnt(2)
	v_mov_b32_e32 v68, v55
	s_waitcnt lgkmcnt(1)
	v_mov_b32_e32 v66, v59
	s_waitcnt lgkmcnt(0)
	v_mov_b32_e32 v70, v63
	s_waitcnt vmcnt(7)
	v_pk_fma_f32 v[4:5], v[18:19], v[48:49], v[4:5] op_sel_hi:[1,0,1]
	v_pk_fma_f32 v[2:3], v[16:17], v[48:49], v[2:3] op_sel_hi:[1,0,1]
	v_pk_fma_f32 v[8:9], v[18:19], v[56:57], v[8:9] op_sel_hi:[1,0,1]
	v_pk_fma_f32 v[6:7], v[16:17], v[56:57], v[6:7] op_sel_hi:[1,0,1]
	s_waitcnt vmcnt(6)
	v_pk_fma_f32 v[2:3], v[20:21], v[48:49], v[2:3] op_sel:[0,1,0]
	v_pk_fma_f32 v[4:5], v[22:23], v[48:49], v[4:5] op_sel:[0,1,0]
	v_pk_fma_f32 v[6:7], v[20:21], v[56:57], v[6:7] op_sel:[0,1,0]
	v_pk_fma_f32 v[8:9], v[22:23], v[56:57], v[8:9] op_sel:[0,1,0]
	s_waitcnt vmcnt(5)
	v_pk_fma_f32 v[4:5], v[26:27], v[50:51], v[4:5] op_sel_hi:[1,0,1]
	v_pk_fma_f32 v[2:3], v[24:25], v[50:51], v[2:3] op_sel_hi:[1,0,1]
	v_pk_fma_f32 v[8:9], v[26:27], v[58:59], v[8:9] op_sel_hi:[1,0,1]
	v_pk_fma_f32 v[6:7], v[24:25], v[58:59], v[6:7] op_sel_hi:[1,0,1]
	s_waitcnt vmcnt(4)
	v_pk_fma_f32 v[4:5], v[30:31], v[64:65], v[4:5] op_sel_hi:[1,0,1]
	v_pk_fma_f32 v[2:3], v[28:29], v[64:65], v[2:3] op_sel_hi:[1,0,1]
	v_pk_fma_f32 v[8:9], v[30:31], v[66:67], v[8:9] op_sel_hi:[1,0,1]
	v_pk_fma_f32 v[6:7], v[28:29], v[66:67], v[6:7] op_sel_hi:[1,0,1]
	s_waitcnt vmcnt(3)
	v_pk_fma_f32 v[4:5], v[34:35], v[52:53], v[4:5] op_sel_hi:[1,0,1]
	v_pk_fma_f32 v[2:3], v[32:33], v[52:53], v[2:3] op_sel_hi:[1,0,1]
	v_pk_fma_f32 v[8:9], v[34:35], v[60:61], v[8:9] op_sel_hi:[1,0,1]
	v_pk_fma_f32 v[6:7], v[32:33], v[60:61], v[6:7] op_sel_hi:[1,0,1]
	s_waitcnt vmcnt(2)
	v_pk_fma_f32 v[4:5], v[38:39], v[52:53], v[4:5] op_sel:[0,1,0]
	v_pk_fma_f32 v[2:3], v[36:37], v[52:53], v[2:3] op_sel:[0,1,0]
	v_pk_fma_f32 v[8:9], v[38:39], v[60:61], v[8:9] op_sel:[0,1,0]
	v_pk_fma_f32 v[6:7], v[36:37], v[60:61], v[6:7] op_sel:[0,1,0]
	s_waitcnt vmcnt(1)
	v_pk_fma_f32 v[4:5], v[42:43], v[54:55], v[4:5] op_sel_hi:[1,0,1]
	v_pk_fma_f32 v[2:3], v[40:41], v[54:55], v[2:3] op_sel_hi:[1,0,1]
	v_pk_fma_f32 v[8:9], v[42:43], v[62:63], v[8:9] op_sel_hi:[1,0,1]
	v_pk_fma_f32 v[6:7], v[40:41], v[62:63], v[6:7] op_sel_hi:[1,0,1]
	s_waitcnt vmcnt(0)
	v_pk_fma_f32 v[4:5], v[46:47], v[68:69], v[4:5] op_sel_hi:[1,0,1]
	v_pk_fma_f32 v[2:3], v[44:45], v[68:69], v[2:3] op_sel_hi:[1,0,1]
	v_pk_fma_f32 v[8:9], v[46:47], v[70:71], v[8:9] op_sel_hi:[1,0,1]
	v_pk_fma_f32 v[6:7], v[44:45], v[70:71], v[6:7] op_sel_hi:[1,0,1]
	s_cbranch_scc0 .LBB0_20
	ds_write_b128 v15, v[2:5] offset:16384
	ds_write_b128 v15, v[6:9] offset:17408
	s_waitcnt lgkmcnt(0)
	s_barrier
	ds_read2st64_b32 v[2:3], v14 offset0:64 offset1:72
	ds_read2st64_b32 v[4:5], v14 offset0:80 offset1:88
	ds_read2st64_b32 v[6:7], v14 offset0:96 offset1:104
	s_add_i32 s19, s19, s33
	s_cmpk_gt_i32 s19, 0x17f
	s_waitcnt lgkmcnt(2)
	v_add_f32_e32 v2, 0, v2
	v_add_f32_e32 v8, v2, v3
	ds_read2st64_b32 v[2:3], v14 offset0:112 offset1:120
	s_waitcnt lgkmcnt(2)
	v_add_f32_e32 v4, v8, v4
	v_add_f32_e32 v4, v4, v5
	s_waitcnt lgkmcnt(1)
	v_add_f32_e32 v4, v4, v6
	v_add_f32_e32 v4, v4, v7
	s_waitcnt lgkmcnt(0)
	v_add_f32_e32 v2, v4, v2
	v_add_f32_e32 v4, v2, v3
	v_lshl_or_b32 v2, s20, 1, v1
	v_mul_lo_u32 v2, v2, s18
	v_add_u32_e32 v2, s6, v2
	v_or_b32_sdwa v2, v2, v0 dst_sel:DWORD dst_unused:UNUSED_PAD src0_sel:DWORD src1_sel:BYTE_0
	v_ashrrev_i32_e32 v3, 31, v2
	v_lshl_add_u64 v[2:3], v[2:3], 2, s[0:1]
	global_store_dword v[2:3], v4, off
	s_barrier
	s_cbranch_scc0 .LBB0_19

.LBB0_104:
	s_waitcnt lgkmcnt(5)
	global_load_dwordx4 v[6:9], v[42:43], off offset:-4096 nt
	s_waitcnt lgkmcnt(3)
	global_load_dwordx4 v[10:13], v[42:43], off offset:-3072 nt
	s_waitcnt lgkmcnt(0)
	global_load_dwordx4 v[18:21], v[42:43], off offset:-2048 nt
	global_load_dwordx4 v[22:25], v[42:43], off offset:-1024 nt
	global_load_dwordx4 v[30:33], v[42:43], off nt
	global_load_dwordx4 v[26:29], v[42:43], off offset:1024 nt
	global_load_dwordx4 v[14:17], v[42:43], off offset:2048 nt
	global_load_dwordx4 v[2:5], v[42:43], off offset:3072 nt
	v_cmp_lt_i32_e32 vcc, v63, v62
	s_mov_b32 s82, 0x800000
	s_and_b32 s75, s0, 0xffffe000
	v_cndmask_b32_e32 v45, v34, v63, vcc
	v_lshlrev_b32_e32 v45, 2, v45
	v_cmp_lt_i32_e32 vcc, v64, v62
	v_add_u32_e32 v78, s75, v61
	s_waitcnt vmcnt(7)
	v_mul_f32_e32 v74, v7, v7
	s_waitcnt vmcnt(6)
	v_mul_f32_e32 v75, v11, v11
	s_waitcnt vmcnt(5)
	v_mul_f32_e32 v76, v19, v19
	v_fmac_f32_e32 v74, v6, v6
	s_waitcnt vmcnt(3)
	v_mov_b32_e32 v48, v31
	s_waitcnt vmcnt(2)
	v_mov_b32_e32 v49, v27
	v_fmac_f32_e32 v75, v10, v10
	v_mul_f32_e32 v77, v23, v23
	v_mov_b32_e32 v46, v30
	v_mov_b32_e32 v47, v26
	v_fmac_f32_e32 v76, v18, v18
	v_pk_mul_f32 v[48:49], v[48:49], v[48:49]
	v_fmac_f32_e32 v74, v8, v8
	v_fmac_f32_e32 v75, v12, v12
	v_mov_b32_e32 v50, v32
	v_mov_b32_e32 v51, v28
	v_fmac_f32_e32 v77, v22, v22
	v_fmac_f32_e32 v76, v20, v20
	v_pk_fma_f32 v[46:47], v[46:47], v[46:47], v[48:49]
	v_fmac_f32_e32 v74, v9, v9
	v_fmac_f32_e32 v75, v13, v13
	s_waitcnt vmcnt(1)
	v_mov_b32_e32 v56, v15
	s_waitcnt vmcnt(0)
	v_mov_b32_e32 v57, v3
	v_fmac_f32_e32 v77, v24, v24
	v_fmac_f32_e32 v76, v21, v21
	v_pk_fma_f32 v[46:47], v[50:51], v[50:51], v[46:47]
	v_add_f32_e32 v50, v74, v75
	v_mov_b32_e32 v52, v33
	v_mov_b32_e32 v53, v29
	v_mov_b32_e32 v54, v14
	v_mov_b32_e32 v55, v2
	v_pk_mul_f32 v[56:57], v[56:57], v[56:57]
	v_fmac_f32_e32 v77, v25, v25
	v_add_f32_e32 v50, v50, v76
	v_mov_b32_e32 v58, v16
	v_mov_b32_e32 v59, v4
	v_pk_fma_f32 v[48:49], v[54:55], v[54:55], v[56:57]
	v_pk_fma_f32 v[46:47], v[52:53], v[52:53], v[46:47]
	v_add_f32_e32 v50, v50, v77
	v_mov_b32_e32 v72, v17
	v_mov_b32_e32 v73, v5
	v_pk_fma_f32 v[48:49], v[58:59], v[58:59], v[48:49]
	v_add_f32_e32 v46, v50, v46
	v_pk_fma_f32 v[48:49], v[72:73], v[72:73], v[48:49]
	v_add_f32_e32 v46, v46, v47
	v_add_f32_e32 v46, v46, v48
	v_add_f32_e32 v46, v46, v49
	ds_bpermute_b32 v47, v45, v46
	v_cndmask_b32_e32 v48, v34, v64, vcc
	v_lshlrev_b32_e32 v72, 2, v48
	v_cmp_lt_i32_e32 vcc, v65, v62
	v_add_u32_e32 v77, s75, v60
	s_waitcnt lgkmcnt(0)
	v_add_f32_e32 v46, v46, v47
	ds_bpermute_b32 v47, v72, v46
	v_cndmask_b32_e32 v49, v34, v65, vcc
	v_lshlrev_b32_e32 v73, 2, v49
	v_cmp_lt_i32_e32 vcc, v66, v62
	ds_read_b128 v[80:83], v77
	ds_read_b128 v[84:87], v77 offset:1024
	ds_read_b128 v[88:91], v78
	ds_read_b128 v[92:95], v78 offset:1024
	s_waitcnt lgkmcnt(4)
	v_add_f32_e32 v46, v46, v47
	s_nop 1
	v_mov_b32_dpp v47, v46 row_ror:8 row_mask:0xf bank_mask:0xf
	v_cndmask_b32_e32 v48, v34, v66, vcc
	v_lshlrev_b32_e32 v76, 2, v48
	v_cmp_lt_i32_e32 vcc, v67, v62
	ds_read_b128 v[96:99], v77 offset:2048
	ds_read_b128 v[100:103], v77 offset:3072
	ds_read_b128 v[104:107], v78 offset:2048
	ds_read_b128 v[108:111], v78 offset:3072
	s_waitcnt lgkmcnt(4)
	v_add_f32_e32 v46, v46, v47
	s_nop 1
	v_mov_b32_dpp v47, v46 row_ror:4 row_mask:0xf bank_mask:0xf
	v_cndmask_b32_e32 v50, v34, v67, vcc
	v_lshlrev_b32_e32 v75, 2, v50
	v_cmp_lt_i32_e32 vcc, v68, v62
	ds_read_b128 v[112:115], v77 offset:4096
	ds_read_b128 v[116:119], v77 offset:5120
	ds_read_b128 v[120:123], v78 offset:4096
	ds_read_b128 v[124:127], v78 offset:5120
	s_waitcnt lgkmcnt(4)
	v_add_f32_e32 v46, v46, v47
	s_nop 1
	v_mov_b32_dpp v47, v46 quad_perm:[2,3,0,1] row_mask:0xf bank_mask:0xf
	v_cndmask_b32_e32 v49, v34, v68, vcc
	v_lshlrev_b32_e32 v74, 2, v49
	s_waitcnt lgkmcnt(0)
	v_add_f32_e32 v46, v46, v47
	s_nop 1
	v_mov_b32_dpp v47, v46 quad_perm:[1,0,3,2] row_mask:0xf bank_mask:0xf
	s_waitcnt lgkmcnt(0)
	v_add_f32_e32 v46, v46, v47
	v_fmamk_f32 v46, v46, 0x3a000000, v69
	v_mul_f32_e32 v47, 0x4b800000, v46
	v_cmp_gt_f32_e32 vcc, s82, v46
	s_nop 1
	v_cndmask_b32_e32 v46, v46, v47, vcc
	v_rsq_f32_e32 v46, v46
	s_nop 0
	v_mul_f32_e32 v47, 0x45800000, v46
	v_cndmask_b32_e32 v128, v46, v47, vcc
	v_pk_mul_f32 v[56:57], v[8:9], v[128:129] op_sel_hi:[1,0]
	v_pk_mul_f32 v[58:59], v[6:7], v[128:129] op_sel_hi:[1,0]
	v_pk_mul_f32 v[52:53], v[12:13], v[128:129] op_sel_hi:[1,0]
	v_pk_mul_f32 v[54:55], v[10:11], v[128:129] op_sel_hi:[1,0]
	v_pk_fma_f32 v[6:7], v[82:83], v[56:57], v[90:91]
	v_pk_fma_f32 v[8:9], v[80:81], v[58:59], v[88:89]
	v_pk_mul_f32 v[48:49], v[20:21], v[128:129] op_sel_hi:[1,0]
	v_pk_mul_f32 v[50:51], v[18:19], v[128:129] op_sel_hi:[1,0]
	v_pk_mul_f32 v[18:19], v[26:27], v[128:129] op_sel_hi:[1,0]
	v_pk_fma_f32 v[10:11], v[86:87], v[52:53], v[94:95]
	v_pk_fma_f32 v[26:27], v[84:85], v[54:55], v[92:93]
	v_max_f32_e64 v8, |v8|, |v9|
	v_max_f32_e64 v6, |v6|, |v7|
	v_pk_mul_f32 v[24:25], v[24:25], v[128:129] op_sel_hi:[1,0]
	v_pk_mul_f32 v[46:47], v[22:23], v[128:129] op_sel_hi:[1,0]
	v_pk_mul_f32 v[22:23], v[30:31], v[128:129] op_sel_hi:[1,0]
	v_pk_mul_f32 v[12:13], v[28:29], v[128:129] op_sel_hi:[1,0]
	v_pk_fma_f32 v[28:29], v[98:99], v[48:49], v[106:107]
	v_pk_fma_f32 v[30:31], v[96:97], v[50:51], v[104:105]
	v_max_f32_e64 v7, |v26|, |v27|
	v_max_f32_e64 v9, |v10|, |v11|
	v_max3_f32 v6, v8, 0, v6
	v_pk_mul_f32 v[20:21], v[32:33], v[128:129] op_sel_hi:[1,0]
	v_pk_fma_f32 v[32:33], v[102:103], v[24:25], v[110:111]
	v_pk_fma_f32 v[80:81], v[100:101], v[46:47], v[108:109]
	v_max_f32_e64 v10, |v30|, |v31|
	v_max_f32_e64 v11, |v28|, |v29|
	v_max3_f32 v6, v6, v7, v9
	v_pk_fma_f32 v[82:83], v[114:115], v[20:21], v[122:123]
	v_pk_fma_f32 v[84:85], v[112:113], v[22:23], v[120:121]
	v_max_f32_e64 v26, |v80|, |v81|
	v_max_f32_e64 v27, |v32|, |v33|
	v_max3_f32 v6, v6, v10, v11
	v_max_f32_e64 v28, |v84|, |v85|
	v_max_f32_e64 v29, |v82|, |v83|
	v_max3_f32 v6, v6, v26, v27
	v_max3_f32 v10, v6, v28, v29
	ds_read_b128 v[26:29], v77 offset:6144
	ds_read_b128 v[30:33], v78 offset:6144
	v_pk_fma_f32 v[6:7], v[118:119], v[12:13], v[126:127]
	v_pk_fma_f32 v[8:9], v[116:117], v[18:19], v[124:125]
	v_max_f32_e64 v6, |v6|, |v7|
	v_max_f32_e64 v8, |v8|, |v9|
	v_max3_f32 v79, v10, v8, v6
	v_pk_mul_f32 v[8:9], v[16:17], v[128:129] op_sel_hi:[1,0]
	v_pk_mul_f32 v[10:11], v[14:15], v[128:129] op_sel_hi:[1,0]
	ds_read_b128 v[14:17], v77 offset:7168
	ds_read_b128 v[80:83], v78 offset:7168
	s_waitcnt lgkmcnt(2)
	v_pk_fma_f32 v[6:7], v[28:29], v[8:9], v[32:33]
	v_pk_fma_f32 v[26:27], v[26:27], v[10:11], v[30:31]
	v_max_f32_e64 v6, |v6|, |v7|
	v_max_f32_e64 v26, |v26|, |v27|
	v_max3_f32 v26, v79, v26, v6
	v_pk_mul_f32 v[4:5], v[4:5], v[128:129] op_sel_hi:[1,0]
	v_pk_mul_f32 v[6:7], v[2:3], v[128:129] op_sel_hi:[1,0]
	s_waitcnt lgkmcnt(0)
	v_pk_fma_f32 v[2:3], v[4:5], v[16:17], v[82:83]
	v_pk_fma_f32 v[14:15], v[6:7], v[14:15], v[80:81]
	v_max_f32_e64 v2, |v2|, |v3|
	v_max_f32_e64 v14, |v14|, |v15|
	v_max3_f32 v2, v26, v14, v2
	ds_bpermute_b32 v3, v45, v2
	s_waitcnt lgkmcnt(0)
	v_max_f32_e32 v3, v3, v3
	v_max_f32_e32 v2, v2, v3
	ds_bpermute_b32 v3, v72, v2
	s_waitcnt lgkmcnt(0)
	v_max_f32_e32 v3, v3, v3
	v_max_f32_e32 v2, v2, v3
	s_nop 1
	v_mov_b32_dpp v3, v2 row_ror:8 row_mask:0xf bank_mask:0xf
	s_waitcnt lgkmcnt(0)
	v_max_f32_e32 v3, v3, v3
	v_max_f32_e32 v2, v2, v3
	s_nop 1
	v_mov_b32_dpp v3, v2 row_ror:4 row_mask:0xf bank_mask:0xf
	s_waitcnt lgkmcnt(0)
	v_max_f32_e32 v3, v3, v3
	v_max_f32_e32 v2, v2, v3
	s_nop 1
	v_mov_b32_dpp v3, v2 quad_perm:[2,3,0,1] row_mask:0xf bank_mask:0xf
	s_waitcnt lgkmcnt(0)
	v_max_f32_e32 v3, v3, v3
	v_max_f32_e32 v2, v2, v3
	s_nop 1
	v_mov_b32_dpp v3, v2 quad_perm:[1,0,3,2] row_mask:0xf bank_mask:0xf
	s_waitcnt lgkmcnt(0)
	v_max_f32_e32 v3, v3, v3
	v_max_f32_e32 v2, v2, v3
	s_and_saveexec_b64 s[82:83], s[6:7]
	s_cbranch_execz .LBB0_106
	s_add_u32 s86, s76, s25
	s_addc_u32 s87, s77, s34
	v_mul_f32_e32 v3, 0x3c010204, v2
	global_store_dword v35, v3, s[86:87]

.LBB0_399:
	v_ashrrev_i32_e32 v4, 13, v1
	v_lshlrev_b32_e32 v2, 1, v1
	v_ashrrev_i32_e32 v5, 31, v4
	v_and_b32_e32 v8, 0x7e, v2
	v_lshlrev_b64 v[12:13], 21, v[4:5]
	v_and_b32_e32 v2, 0x3f80, v2
	v_or3_b32 v6, v12, v2, v8
	v_mov_b32_e32 v7, v13
	v_lshl_add_u64 v[22:23], v[6:7], 1, s[4:5]
	v_add_co_u32_e32 v26, vcc, s18, v22
	v_lshlrev_b64 v[4:5], 16, v[4:5]
	s_nop 0
	v_addc_co_u32_e32 v27, vcc, 0, v23, vcc
	v_add_co_u32_e32 v28, vcc, s19, v22
	v_lshl_add_u64 v[6:7], s[6:7], 0, v[4:5]
	s_nop 0
	v_addc_co_u32_e32 v29, vcc, 0, v23, vcc
	v_add_co_u32_e32 v30, vcc, s21, v22
	v_lshlrev_b32_e32 v2, 2, v8
	s_nop 0
	v_addc_co_u32_e32 v31, vcc, 0, v23, vcc
	v_add_co_u32_e32 v32, vcc, s16, v22
	v_lshl_add_u64 v[24:25], v[6:7], 0, v[2:3]
	s_nop 0
	v_addc_co_u32_e32 v33, vcc, 0, v23, vcc
	v_add_co_u32_e32 v34, vcc, s22, v22
	global_load_dword v2, v[22:23], off nt
	global_load_dwordx2 v[6:7], v[24:25], off
	global_load_dwordx2 v[8:9], v[24:25], off offset:512
	global_load_dwordx2 v[10:11], v[24:25], off offset:1024
	v_addc_co_u32_e32 v35, vcc, 0, v23, vcc
	v_add_co_u32_e32 v36, vcc, s23, v22
	global_load_dwordx2 v[14:15], v[24:25], off offset:1536
	global_load_dwordx2 v[16:17], v[24:25], off offset:2048
	global_load_dwordx2 v[18:19], v[24:25], off offset:2560
	global_load_dwordx2 v[20:21], v[24:25], off offset:3072
	v_addc_co_u32_e32 v37, vcc, 0, v23, vcc
	v_add_co_u32_e32 v22, vcc, s25, v22
	s_mov_b32 s69, 0
	s_nop 0
	v_addc_co_u32_e32 v23, vcc, 0, v23, vcc
	global_load_dword v49, v[26:27], off nt
	global_load_dword v50, v[28:29], off nt
	global_load_dword v51, v[30:31], off nt
	global_load_dword v52, v[32:33], off nt
	global_load_dword v53, v[34:35], off nt
	global_load_dword v54, v[36:37], off nt
	global_load_dword v56, v[22:23], off nt
	s_nop 0
	global_load_dwordx2 v[24:25], v[24:25], off offset:3584
	v_and_b32_e32 v23, 0x3f80, v48
	v_and_b32_e32 v26, 0x7e, v48
	v_lshlrev_b32_e32 v22, 2, v48
	v_or3_b32 v12, v12, v23, v26
	v_and_or_b32 v4, v22, s26, v4
	v_lshlrev_b64 v[12:13], 1, v[12:13]
	v_mov_b32_e32 v46, 0
	v_mov_b32_e32 v47, v3
	s_waitcnt vmcnt(1)
	v_mov_b32_e32 v55, v56
	s_branch .LBB0_401

.LBB0_401:
	v_lshl_add_u64 v[22:23], s[76:77], 0, v[12:13]
	v_add_co_u32_e32 v26, vcc, s27, v22
	v_lshl_add_u64 v[44:45], s[76:77], 0, v[4:5]
	s_nop 0
	v_addc_co_u32_e32 v27, vcc, 0, v23, vcc
	v_add_co_u32_e32 v42, vcc, s28, v44
	s_cmpk_gt_u32 s69, 0x6f
	s_nop 0
	v_addc_co_u32_e32 v43, vcc, 0, v45, vcc
	v_add_co_u32_e32 v58, vcc, s29, v22
	global_load_dword v62, v[26:27], off nt
	global_load_dwordx2 v[40:41], v[42:43], off
	global_load_dwordx2 v[38:39], v[42:43], off offset:512
	global_load_dwordx2 v[34:35], v[42:43], off offset:1024
	v_addc_co_u32_e32 v59, vcc, 0, v23, vcc
	v_add_co_u32_e32 v60, vcc, s30, v22
	global_load_dwordx2 v[36:37], v[42:43], off offset:1536
	global_load_dwordx2 v[32:33], v[42:43], off offset:2048
	global_load_dwordx2 v[30:31], v[42:43], off offset:2560
	global_load_dwordx2 v[28:29], v[42:43], off offset:3072
	v_addc_co_u32_e32 v61, vcc, 0, v23, vcc
	v_add_co_u32_e32 v26, vcc, s31, v22
	s_cselect_b64 s[14:15], -1, 0
	s_nop 0
	v_addc_co_u32_e32 v27, vcc, 0, v23, vcc
	v_add_co_u32_e32 v66, vcc, s34, v22
	s_cmpk_lt_u32 s69, 0x70
	s_nop 0
	v_addc_co_u32_e32 v67, vcc, 0, v23, vcc
	v_add_co_u32_e32 v68, vcc, s35, v22
	s_nop 1
	v_addc_co_u32_e32 v69, vcc, 0, v23, vcc
	v_add_co_u32_e32 v70, vcc, s42, v22
	s_nop 1
	v_addc_co_u32_e32 v71, vcc, 0, v23, vcc
	v_add_co_u32_e32 v72, vcc, s43, v22
	s_nop 1
	v_addc_co_u32_e32 v73, vcc, 0, v23, vcc
	global_load_dword v64, v[58:59], off nt
	global_load_dword v63, v[60:61], off nt
	s_nop 0
	global_load_dword v61, v[26:27], off nt
	global_load_dword v60, v[66:67], off nt
	global_load_dword v59, v[68:69], off nt
	global_load_dword v58, v[70:71], off nt
	global_load_dword v57, v[72:73], off nt
	s_nop 0
	global_load_dwordx2 v[26:27], v[42:43], off offset:3584
	v_add_co_u32_e32 v42, vcc, s48, v22
	v_cvt_pk_bf16_f32 v65, v46, v47
	s_nop 1
	v_addc_co_u32_e32 v43, vcc, 0, v23, vcc
	global_store_dword v[42:43], v65, off
	v_lshlrev_b32_e32 v42, 16, v2
	v_and_b32_e32 v43, 0xffff0000, v2
	v_pk_fma_f32 v[42:43], v[46:47], v[6:7], v[42:43]
	v_add_co_u32_e32 v46, vcc, s49, v22
	v_cvt_pk_bf16_f32 v65, v42, v43
	s_nop 1
	v_addc_co_u32_e32 v47, vcc, 0, v23, vcc
	global_store_dword v[46:47], v65, off
	v_lshlrev_b32_e32 v46, 16, v49
	v_and_b32_e32 v47, 0xffff0000, v49
	v_pk_fma_f32 v[42:43], v[8:9], v[42:43], v[46:47]
	v_add_co_u32_e32 v46, vcc, s54, v22
	v_cvt_pk_bf16_f32 v65, v42, v43
	s_nop 1
	v_addc_co_u32_e32 v47, vcc, 0, v23, vcc
	global_store_dword v[46:47], v65, off
	v_lshlrev_b32_e32 v46, 16, v50
	v_and_b32_e32 v47, 0xffff0000, v50
	v_pk_fma_f32 v[42:43], v[10:11], v[42:43], v[46:47]
	v_add_co_u32_e32 v46, vcc, s55, v22
	v_cvt_pk_bf16_f32 v65, v42, v43
	s_nop 1
	v_addc_co_u32_e32 v47, vcc, 0, v23, vcc
	global_store_dword v[46:47], v65, off
	v_lshlrev_b32_e32 v46, 16, v51
	v_and_b32_e32 v47, 0xffff0000, v51
	v_pk_fma_f32 v[42:43], v[14:15], v[42:43], v[46:47]
	v_add_co_u32_e32 v46, vcc, s56, v22
	v_cvt_pk_bf16_f32 v65, v42, v43
	s_nop 1
	v_addc_co_u32_e32 v47, vcc, 0, v23, vcc
	global_store_dword v[46:47], v65, off
	v_lshlrev_b32_e32 v46, 16, v52
	v_and_b32_e32 v47, 0xffff0000, v52
	v_pk_fma_f32 v[42:43], v[16:17], v[42:43], v[46:47]
	v_add_co_u32_e32 v46, vcc, s57, v22
	v_cvt_pk_bf16_f32 v65, v42, v43
	s_nop 1
	v_addc_co_u32_e32 v47, vcc, 0, v23, vcc
	global_store_dword v[46:47], v65, off
	v_lshlrev_b32_e32 v46, 16, v53
	v_and_b32_e32 v47, 0xffff0000, v53
	v_pk_fma_f32 v[42:43], v[18:19], v[42:43], v[46:47]
	v_add_co_u32_e32 v46, vcc, s58, v22
	v_cvt_pk_bf16_f32 v65, v42, v43
	s_nop 1
	v_addc_co_u32_e32 v47, vcc, 0, v23, vcc
	global_store_dword v[46:47], v65, off
	v_lshlrev_b32_e32 v46, 16, v54
	v_and_b32_e32 v47, 0xffff0000, v54
	v_pk_fma_f32 v[46:47], v[20:21], v[42:43], v[46:47]
	v_add_co_u32_e32 v42, vcc, 0x4c620000, v22
	v_cvt_pk_bf16_f32 v65, v46, v47
	s_nop 1
	v_addc_co_u32_e32 v43, vcc, 0, v23, vcc
	global_store_dword v[42:43], v65, off
	s_waitcnt vmcnt(24)
	v_mov_b32_e32 v42, v24
	v_mov_b32_e32 v43, v25
	s_cbranch_scc0 .LBB0_400
	v_add_co_u32_e32 v6, vcc, 0x44668000, v22
	s_nop 1
	v_addc_co_u32_e32 v7, vcc, 0, v23, vcc
	v_add_co_u32_e32 v42, vcc, 0x505ea000, v44
	s_nop 1
	v_addc_co_u32_e32 v43, vcc, 0, v45, vcc
	v_add_co_u32_e32 v44, vcc, 0x44670000, v22
	global_load_dword v2, v[6:7], off nt
	s_nop 0
	global_load_dwordx2 v[6:7], v[42:43], off
	global_load_dwordx2 v[8:9], v[42:43], off offset:512
	global_load_dwordx2 v[10:11], v[42:43], off offset:1024
	v_addc_co_u32_e32 v45, vcc, 0, v23, vcc
	v_add_co_u32_e32 v50, vcc, 0x44678000, v22
	global_load_dwordx2 v[14:15], v[42:43], off offset:1536
	global_load_dwordx2 v[16:17], v[42:43], off offset:2048
	global_load_dwordx2 v[18:19], v[42:43], off offset:2560
	global_load_dwordx2 v[20:21], v[42:43], off offset:3072
	v_addc_co_u32_e32 v51, vcc, 0, v23, vcc
	v_add_co_u32_e32 v52, vcc, 0x44680000, v22
	s_nop 1
	v_addc_co_u32_e32 v53, vcc, 0, v23, vcc
	v_add_co_u32_e32 v54, vcc, 0x44688000, v22
	s_nop 1
	v_addc_co_u32_e32 v55, vcc, 0, v23, vcc
	v_add_co_u32_e32 v66, vcc, 0x44690000, v22
	s_nop 1
	v_addc_co_u32_e32 v67, vcc, 0, v23, vcc
	v_add_co_u32_e32 v68, vcc, 0x44698000, v22
	s_nop 1
	v_addc_co_u32_e32 v69, vcc, 0, v23, vcc
	v_add_co_u32_e32 v70, vcc, 0x446a0000, v22
	s_nop 1
	v_addc_co_u32_e32 v71, vcc, 0, v23, vcc
	global_load_dword v49, v[44:45], off nt
	s_nop 0
	global_load_dword v50, v[50:51], off nt
	s_nop 0
	global_load_dword v51, v[52:53], off nt
	s_nop 0
	global_load_dword v52, v[54:55], off nt
	global_load_dword v53, v[66:67], off nt
	s_nop 0
	global_load_dword v54, v[68:69], off nt
	global_load_dword v55, v[70:71], off nt
	s_nop 0
	global_load_dwordx2 v[42:43], v[42:43], off offset:3584
	s_branch .LBB0_400

.LBB0_616:
	s_lshr_b32 s21, s26, 5
	s_mul_i32 s28, s21, 0x3000
	s_ashr_i32 s29, s28, 31
	v_lshl_or_b32 v242, s27, 8, v233
	s_lshl_b64 s[28:29], s[28:29], 2
	s_add_u32 s28, s49, s28
	v_ashrrev_i32_e32 v243, 31, v242
	s_addc_u32 s29, s54, s29
	v_lshlrev_b64 v[138:139], 2, v[242:243]
	v_lshl_add_u64 v[140:141], s[28:29], 0, v[138:139]
	v_lshl_add_u64 v[142:143], s[12:13], 0, v[138:139]
	global_load_dwordx4 v[126:129], v[140:141], off
	global_load_dwordx4 v[130:133], v[142:143], off
	global_load_dwordx4 v[146:149], v[140:141], off offset:64
	global_load_dwordx4 v[150:153], v[142:143], off offset:64
	global_load_dwordx4 v[154:157], v[140:141], off offset:512
	global_load_dwordx4 v[158:161], v[142:143], off offset:512
	global_load_dwordx4 v[162:165], v[140:141], off offset:576
	global_load_dwordx4 v[166:169], v[142:143], off offset:576
	v_lshl_add_u32 v224, s26, 8, v1
	v_ashrrev_i32_e32 v225, 31, v224
	v_lshl_add_u64 v[226:227], v[224:225], 2, s[10:11]
	global_load_dword v240, v[226:227], off
	v_lshl_add_u64 v[222:223], s[52:53], 0, v[138:139]
	v_or_b32_e32 v238, 16, v224
	v_ashrrev_i32_e32 v239, 31, v238
	v_or_b32_e32 v234, 32, v224
	v_ashrrev_i32_e32 v235, 31, v234
	v_or_b32_e32 v230, 48, v224
	v_ashrrev_i32_e32 v231, 31, v230
	v_cvt_f32_i32_e32 v135, v135
	v_cvt_f32_i32_e32 v134, v134
	v_cvt_f32_i32_e32 v137, v137
	v_cvt_f32_i32_e32 v136, v136
	v_cvt_f32_i32_e32 v123, v123
	v_cvt_f32_i32_e32 v122, v122
	v_cvt_f32_i32_e32 v125, v125
	v_cvt_f32_i32_e32 v124, v124
	v_lshlrev_b64 v[244:245], 12, v[224:225]
	v_cvt_f32_i32_e32 v119, v119
	v_cvt_f32_i32_e32 v118, v118
	v_cvt_f32_i32_e32 v121, v121
	v_cvt_f32_i32_e32 v120, v120
	v_cvt_f32_i32_e32 v115, v115
	v_cvt_f32_i32_e32 v114, v114
	v_cvt_f32_i32_e32 v117, v117
	v_cvt_f32_i32_e32 v116, v116
	v_cvt_f32_i32_e32 v111, v111
	v_cvt_f32_i32_e32 v110, v110
	v_cvt_f32_i32_e32 v113, v113
	v_cvt_f32_i32_e32 v112, v112
	v_cvt_f32_i32_e32 v107, v107
	v_cvt_f32_i32_e32 v106, v106
	v_cvt_f32_i32_e32 v109, v109
	v_cvt_f32_i32_e32 v108, v108
	v_cvt_f32_i32_e32 v103, v103
	v_cvt_f32_i32_e32 v102, v102
	v_cvt_f32_i32_e32 v105, v105
	v_cvt_f32_i32_e32 v104, v104
	v_cvt_f32_i32_e32 v99, v99
	v_cvt_f32_i32_e32 v98, v98
	v_cvt_f32_i32_e32 v101, v101
	v_cvt_f32_i32_e32 v100, v100
	v_cvt_f32_i32_e32 v95, v95
	v_cvt_f32_i32_e32 v94, v94
	v_cvt_f32_i32_e32 v97, v97
	v_cvt_f32_i32_e32 v96, v96
	v_cvt_f32_i32_e32 v91, v91
	v_cvt_f32_i32_e32 v90, v90
	v_cvt_f32_i32_e32 v93, v93
	v_cvt_f32_i32_e32 v92, v92
	v_cvt_f32_i32_e32 v87, v87
	v_cvt_f32_i32_e32 v86, v86
	v_cvt_f32_i32_e32 v89, v89
	v_cvt_f32_i32_e32 v88, v88
	v_cvt_f32_i32_e32 v83, v83
	v_cvt_f32_i32_e32 v82, v82
	v_cvt_f32_i32_e32 v85, v85
	v_cvt_f32_i32_e32 v84, v84
	v_cvt_f32_i32_e32 v79, v79
	v_cvt_f32_i32_e32 v78, v78
	v_cvt_f32_i32_e32 v81, v81
	v_cvt_f32_i32_e32 v80, v80
	v_cvt_f32_i32_e32 v75, v75
	v_cvt_f32_i32_e32 v74, v74
	v_cvt_f32_i32_e32 v77, v77
	v_cvt_f32_i32_e32 v76, v76
	v_cvt_f32_i32_e32 v71, v71
	v_cvt_f32_i32_e32 v70, v70
	v_cvt_f32_i32_e32 v73, v73
	v_cvt_f32_i32_e32 v72, v72
	v_cvt_f32_i32_e32 v67, v67
	v_cvt_f32_i32_e32 v66, v66
	v_cvt_f32_i32_e32 v69, v69
	v_cvt_f32_i32_e32 v68, v68
	v_cvt_f32_i32_e32 v63, v63
	v_cvt_f32_i32_e32 v62, v62
	v_cvt_f32_i32_e32 v65, v65
	v_cvt_f32_i32_e32 v64, v64
	s_waitcnt vmcnt(0)
	v_pk_mul_f32 v[128:129], v[128:129], v[132:133]
	v_pk_mul_f32 v[126:127], v[126:127], v[130:131]
	v_pk_mul_f32 v[218:219], v[128:129], s[18:19] op_sel_hi:[1,0]
	v_pk_mul_f32 v[220:221], v[126:127], s[18:19] op_sel_hi:[1,0]
	v_cvt_f32_i32_e32 v59, v59
	v_cvt_f32_i32_e32 v58, v58
	v_cvt_f32_i32_e32 v61, v61
	v_cvt_f32_i32_e32 v60, v60
	v_cvt_f32_i32_e32 v55, v55
	v_cvt_f32_i32_e32 v54, v54
	v_cvt_f32_i32_e32 v57, v57
	v_cvt_f32_i32_e32 v56, v56
	v_cvt_f32_i32_e32 v51, v51
	v_cvt_f32_i32_e32 v50, v50
	v_cvt_f32_i32_e32 v53, v53
	v_cvt_f32_i32_e32 v52, v52
	v_cvt_f32_i32_e32 v47, v47
	v_cvt_f32_i32_e32 v46, v46
	v_cvt_f32_i32_e32 v49, v49
	v_cvt_f32_i32_e32 v48, v48
	v_cvt_f32_i32_e32 v43, v43
	v_cvt_f32_i32_e32 v42, v42
	v_cvt_f32_i32_e32 v45, v45
	v_cvt_f32_i32_e32 v44, v44
	v_cvt_f32_i32_e32 v39, v39
	v_cvt_f32_i32_e32 v38, v38
	v_cvt_f32_i32_e32 v41, v41
	v_cvt_f32_i32_e32 v40, v40
	v_cvt_f32_i32_e32 v35, v35
	v_cvt_f32_i32_e32 v34, v34
	v_cvt_f32_i32_e32 v37, v37
	v_cvt_f32_i32_e32 v36, v36
	v_cvt_f32_i32_e32 v31, v31
	v_cvt_f32_i32_e32 v30, v30
	v_cvt_f32_i32_e32 v33, v33
	v_cvt_f32_i32_e32 v32, v32
	v_cvt_f32_i32_e32 v23, v23
	v_cvt_f32_i32_e32 v22, v22
	v_cvt_f32_i32_e32 v25, v25
	v_cvt_f32_i32_e32 v24, v24
	v_cvt_f32_i32_e32 v27, v27
	v_cvt_f32_i32_e32 v26, v26
	v_cvt_f32_i32_e32 v29, v29
	v_cvt_f32_i32_e32 v28, v28
	v_cvt_f32_i32_e32 v19, v19
	v_cvt_f32_i32_e32 v18, v18
	v_cvt_f32_i32_e32 v21, v21
	v_cvt_f32_i32_e32 v20, v20
	v_cvt_f32_i32_e32 v11, v11
	v_cvt_f32_i32_e32 v10, v10
	v_cvt_f32_i32_e32 v13, v13
	v_cvt_f32_i32_e32 v12, v12
	v_cvt_f32_i32_e32 v5, v5
	v_cvt_f32_i32_e32 v4, v4
	v_cvt_f32_i32_e32 v3, v3
	v_cvt_f32_i32_e32 v2, v2
	v_cvt_f32_i32_e32 v7, v7
	v_cvt_f32_i32_e32 v6, v6
	v_cvt_f32_i32_e32 v9, v9
	v_cvt_f32_i32_e32 v8, v8
	s_mov_b64 s[26:27], -1
	s_and_b64 vcc, exec, s[4:5]
	v_pk_mul_f32 v[148:149], v[148:149], v[152:153]
	v_pk_mul_f32 v[146:147], v[146:147], v[150:151]
	v_pk_mul_f32 v[214:215], v[148:149], s[18:19] op_sel_hi:[1,0]
	v_pk_mul_f32 v[216:217], v[146:147], s[18:19] op_sel_hi:[1,0]
	v_pk_mul_f32 v[156:157], v[156:157], v[160:161]
	v_pk_mul_f32 v[154:155], v[154:155], v[158:159]
	v_pk_mul_f32 v[210:211], v[156:157], s[18:19] op_sel_hi:[1,0]
	v_pk_mul_f32 v[212:213], v[154:155], s[18:19] op_sel_hi:[1,0]
	v_pk_mul_f32 v[162:163], v[162:163], v[166:167]
	v_pk_mul_f32 v[164:165], v[164:165], v[168:169]
	v_pk_mul_f32 v[206:207], v[164:165], s[18:19] op_sel_hi:[1,0]
	s_nop 0
	v_pk_mul_f32 v[208:209], v[162:163], s[18:19] op_sel_hi:[1,0]
	v_lshlrev_b64 v[126:127], 13, v[224:225]
	v_lshl_add_u64 v[126:127], v[222:223], 0, v[126:127]
	global_load_dwordx4 v[248:251], v[126:127], off nt
	global_load_dwordx4 v[186:189], v[126:127], off offset:64 nt
	global_load_dwordx4 v[182:185], v[126:127], off offset:512 nt
	global_load_dwordx4 v[178:181], v[126:127], off offset:576 nt
	v_lshl_add_u64 v[126:127], v[238:239], 2, s[10:11]
	global_load_dword v236, v[126:127], off
	v_lshlrev_b64 v[126:127], 13, v[238:239]
	v_lshl_add_u64 v[126:127], v[222:223], 0, v[126:127]
	global_load_dwordx4 v[174:177], v[126:127], off nt
	global_load_dwordx4 v[170:173], v[126:127], off offset:64 nt
	global_load_dwordx4 v[166:169], v[126:127], off offset:512 nt
	global_load_dwordx4 v[162:165], v[126:127], off offset:576 nt
	v_lshl_add_u64 v[126:127], v[234:235], 2, s[10:11]
	global_load_dword v232, v[126:127], off
	v_lshlrev_b64 v[126:127], 13, v[234:235]
	v_lshl_add_u64 v[126:127], v[222:223], 0, v[126:127]
	global_load_dwordx4 v[158:161], v[126:127], off nt
	global_load_dwordx4 v[154:157], v[126:127], off offset:64 nt
	global_load_dwordx4 v[150:153], v[126:127], off offset:512 nt
	global_load_dwordx4 v[146:149], v[126:127], off offset:576 nt
	v_lshl_add_u64 v[126:127], v[230:231], 2, s[10:11]
	global_load_dword v228, v[126:127], off
	v_lshlrev_b64 v[126:127], 13, v[230:231]
	v_lshl_add_u64 v[126:127], v[222:223], 0, v[126:127]
	global_load_dwordx4 v[142:145], v[126:127], off nt
	global_load_dwordx4 v[138:141], v[126:127], off offset:64 nt
	global_load_dwordx4 v[130:133], v[126:127], off offset:512 nt
	s_nop 0
	global_load_dwordx4 v[126:129], v[126:127], off offset:576 nt
	s_waitcnt vmcnt(19)
	v_pk_mul_f32 v[252:253], v[218:219], v[240:241] op_sel_hi:[1,0]
	v_pk_mul_f32 v[204:205], v[220:221], v[240:241] op_sel_hi:[1,0]
	s_waitcnt vmcnt(18)
	v_pk_fma_f32 v[136:137], v[252:253], v[136:137], v[250:251]
	v_pk_fma_f32 v[134:135], v[204:205], v[134:135], v[248:249]
	s_nop 0
	v_cvt_pk_bf16_f32 v204, v134, v135
	v_cvt_pk_bf16_f32 v205, v136, v137
	v_lshl_add_u64 v[136:137], s[8:9], 0, v[244:245]
	v_lshlrev_b64 v[134:135], 1, v[242:243]
	v_pk_mul_f32 v[244:245], v[214:215], v[240:241] op_sel_hi:[1,0]
	v_pk_mul_f32 v[242:243], v[216:217], v[240:241] op_sel_hi:[1,0]
	v_lshl_add_u64 v[136:137], v[136:137], 0, v[134:135]
	s_waitcnt vmcnt(17)
	v_pk_fma_f32 v[124:125], v[244:245], v[124:125], v[188:189]
	v_pk_fma_f32 v[122:123], v[242:243], v[122:123], v[186:187]
	global_store_dwordx2 v[136:137], v[204:205], off
	v_cvt_pk_bf16_f32 v122, v122, v123
	v_cvt_pk_bf16_f32 v123, v124, v125
	v_pk_mul_f32 v[124:125], v[212:213], v[240:241] op_sel_hi:[1,0]
	global_store_dwordx2 v[136:137], v[122:123], off offset:32
	v_pk_mul_f32 v[122:123], v[210:211], v[240:241] op_sel_hi:[1,0]
	s_waitcnt vmcnt(18)
	v_pk_fma_f32 v[118:119], v[124:125], v[118:119], v[182:183]
	v_pk_fma_f32 v[120:121], v[122:123], v[120:121], v[184:185]
	v_cvt_pk_bf16_f32 v118, v118, v119
	s_nop 0
	v_cvt_pk_bf16_f32 v119, v120, v121
	global_store_dwordx2 v[136:137], v[118:119], off offset:256
	v_pk_mul_f32 v[118:119], v[206:207], v[240:241] op_sel_hi:[1,0]
	v_pk_mul_f32 v[120:121], v[208:209], v[240:241] op_sel_hi:[1,0]
	s_waitcnt vmcnt(18)
	v_pk_fma_f32 v[116:117], v[118:119], v[116:117], v[180:181]
	v_pk_fma_f32 v[114:115], v[120:121], v[114:115], v[178:179]
	s_waitcnt vmcnt(17)
	v_pk_mul_f32 v[118:119], v[220:221], v[236:237] op_sel_hi:[1,0]
	v_cvt_pk_bf16_f32 v114, v114, v115
	v_cvt_pk_bf16_f32 v115, v116, v117
	v_pk_mul_f32 v[116:117], v[218:219], v[236:237] op_sel_hi:[1,0]
	global_store_dwordx2 v[136:137], v[114:115], off offset:288
	v_lshlrev_b64 v[114:115], 12, v[238:239]
	s_waitcnt vmcnt(17)
	v_pk_fma_f32 v[112:113], v[116:117], v[112:113], v[176:177]
	v_pk_fma_f32 v[110:111], v[118:119], v[110:111], v[174:175]
	v_add_u32_e32 v120, 0xa0, v224
	v_cvt_pk_bf16_f32 v110, v110, v111
	v_cvt_pk_bf16_f32 v111, v112, v113
	v_lshl_add_u64 v[112:113], s[8:9], 0, v[114:115]
	v_lshl_add_u64 v[112:113], v[112:113], 0, v[134:135]
	global_store_dwordx2 v[112:113], v[110:111], off
	v_pk_mul_f32 v[110:111], v[214:215], v[236:237] op_sel_hi:[1,0]
	v_pk_mul_f32 v[114:115], v[216:217], v[236:237] op_sel_hi:[1,0]
	s_waitcnt vmcnt(17)
	v_pk_fma_f32 v[108:109], v[110:111], v[108:109], v[172:173]
	v_pk_fma_f32 v[106:107], v[114:115], v[106:107], v[170:171]
	v_ashrrev_i32_e32 v121, 31, v120
	v_cvt_pk_bf16_f32 v106, v106, v107
	v_cvt_pk_bf16_f32 v107, v108, v109
	v_pk_mul_f32 v[108:109], v[212:213], v[236:237] op_sel_hi:[1,0]
	global_store_dwordx2 v[112:113], v[106:107], off offset:32
	v_pk_mul_f32 v[106:107], v[210:211], v[236:237] op_sel_hi:[1,0]
	s_waitcnt vmcnt(17)
	v_pk_fma_f32 v[102:103], v[108:109], v[102:103], v[166:167]
	v_pk_fma_f32 v[104:105], v[106:107], v[104:105], v[168:169]
	v_cvt_pk_bf16_f32 v102, v102, v103
	v_add_u32_e32 v116, 0xb0, v224
	v_cvt_pk_bf16_f32 v103, v104, v105
	global_store_dwordx2 v[112:113], v[102:103], off offset:256
	v_pk_mul_f32 v[102:103], v[206:207], v[236:237] op_sel_hi:[1,0]
	v_pk_mul_f32 v[104:105], v[208:209], v[236:237] op_sel_hi:[1,0]
	s_waitcnt vmcnt(17)
	v_pk_fma_f32 v[100:101], v[102:103], v[100:101], v[164:165]
	v_pk_fma_f32 v[98:99], v[104:105], v[98:99], v[162:163]
	s_waitcnt vmcnt(16)
	v_pk_mul_f32 v[102:103], v[220:221], v[232:233] op_sel_hi:[1,0]
	v_cvt_pk_bf16_f32 v98, v98, v99
	v_cvt_pk_bf16_f32 v99, v100, v101
	v_pk_mul_f32 v[100:101], v[218:219], v[232:233] op_sel_hi:[1,0]
	global_store_dwordx2 v[112:113], v[98:99], off offset:288
	v_lshlrev_b64 v[98:99], 12, v[234:235]
	s_waitcnt vmcnt(16)
	v_pk_fma_f32 v[96:97], v[100:101], v[96:97], v[160:161]
	v_pk_fma_f32 v[94:95], v[102:103], v[94:95], v[158:159]
	v_ashrrev_i32_e32 v117, 31, v116
	v_cvt_pk_bf16_f32 v94, v94, v95
	v_cvt_pk_bf16_f32 v95, v96, v97
	v_lshl_add_u64 v[96:97], s[8:9], 0, v[98:99]
	v_lshl_add_u64 v[96:97], v[96:97], 0, v[134:135]
	global_store_dwordx2 v[96:97], v[94:95], off
	v_pk_mul_f32 v[94:95], v[214:215], v[232:233] op_sel_hi:[1,0]
	v_pk_mul_f32 v[98:99], v[216:217], v[232:233] op_sel_hi:[1,0]
	s_waitcnt vmcnt(16)
	v_pk_fma_f32 v[92:93], v[94:95], v[92:93], v[156:157]
	v_pk_fma_f32 v[90:91], v[98:99], v[90:91], v[154:155]
	s_nop 0
	v_cvt_pk_bf16_f32 v90, v90, v91
	v_cvt_pk_bf16_f32 v91, v92, v93
	v_pk_mul_f32 v[92:93], v[212:213], v[232:233] op_sel_hi:[1,0]
	global_store_dwordx2 v[96:97], v[90:91], off offset:32
	v_pk_mul_f32 v[90:91], v[210:211], v[232:233] op_sel_hi:[1,0]
	s_waitcnt vmcnt(16)
	v_pk_fma_f32 v[86:87], v[92:93], v[86:87], v[150:151]
	v_pk_fma_f32 v[88:89], v[90:91], v[88:89], v[152:153]
	v_cvt_pk_bf16_f32 v86, v86, v87
	s_nop 0
	v_cvt_pk_bf16_f32 v87, v88, v89
	global_store_dwordx2 v[96:97], v[86:87], off offset:256
	v_pk_mul_f32 v[86:87], v[206:207], v[232:233] op_sel_hi:[1,0]
	v_pk_mul_f32 v[88:89], v[208:209], v[232:233] op_sel_hi:[1,0]
	s_waitcnt vmcnt(16)
	v_pk_fma_f32 v[84:85], v[86:87], v[84:85], v[148:149]
	v_pk_fma_f32 v[82:83], v[88:89], v[82:83], v[146:147]
	s_waitcnt vmcnt(15)
	v_pk_mul_f32 v[86:87], v[220:221], v[228:229] op_sel_hi:[1,0]
	v_cvt_pk_bf16_f32 v82, v82, v83
	v_cvt_pk_bf16_f32 v83, v84, v85
	v_pk_mul_f32 v[84:85], v[218:219], v[228:229] op_sel_hi:[1,0]
	global_store_dwordx2 v[96:97], v[82:83], off offset:288
	v_lshlrev_b64 v[82:83], 12, v[230:231]
	s_waitcnt vmcnt(15)
	v_pk_fma_f32 v[80:81], v[84:85], v[80:81], v[144:145]
	v_pk_fma_f32 v[78:79], v[86:87], v[78:79], v[142:143]
	v_add_u32_e32 v146, 0x90, v224
	v_cvt_pk_bf16_f32 v78, v78, v79
	v_cvt_pk_bf16_f32 v79, v80, v81
	v_lshl_add_u64 v[80:81], s[8:9], 0, v[82:83]
	v_lshl_add_u64 v[80:81], v[80:81], 0, v[134:135]
	v_pk_mul_f32 v[82:83], v[216:217], v[228:229] op_sel_hi:[1,0]
	global_store_dwordx2 v[80:81], v[78:79], off
	v_pk_mul_f32 v[78:79], v[214:215], v[228:229] op_sel_hi:[1,0]
	s_waitcnt vmcnt(15)
	v_pk_fma_f32 v[74:75], v[82:83], v[74:75], v[138:139]
	v_pk_fma_f32 v[76:77], v[78:79], v[76:77], v[140:141]
	v_cvt_pk_bf16_f32 v74, v74, v75
	v_ashrrev_i32_e32 v147, 31, v146
	v_cvt_pk_bf16_f32 v75, v76, v77
	global_store_dwordx2 v[80:81], v[74:75], off offset:32
	v_pk_mul_f32 v[74:75], v[210:211], v[228:229] op_sel_hi:[1,0]
	v_pk_mul_f32 v[76:77], v[212:213], v[228:229] op_sel_hi:[1,0]
	s_waitcnt vmcnt(15)
	v_pk_fma_f32 v[72:73], v[74:75], v[72:73], v[132:133]
	v_pk_fma_f32 v[70:71], v[76:77], v[70:71], v[130:131]
	v_add_u32_e32 v132, 0x80, v224
	v_cvt_pk_bf16_f32 v70, v70, v71
	v_cvt_pk_bf16_f32 v71, v72, v73
	v_pk_mul_f32 v[72:73], v[208:209], v[228:229] op_sel_hi:[1,0]
	global_store_dwordx2 v[80:81], v[70:71], off offset:256
	v_pk_mul_f32 v[70:71], v[206:207], v[228:229] op_sel_hi:[1,0]
	s_waitcnt vmcnt(15)
	v_pk_fma_f32 v[66:67], v[72:73], v[66:67], v[126:127]
	v_pk_fma_f32 v[68:69], v[70:71], v[68:69], v[128:129]
	v_cvt_pk_bf16_f32 v66, v66, v67
	v_ashrrev_i32_e32 v133, 31, v132
	v_cvt_pk_bf16_f32 v67, v68, v69
	global_store_dwordx2 v[80:81], v[66:67], off offset:288
	global_load_dword v144, v[226:227], off offset:512
	v_lshlrev_b64 v[66:67], 13, v[132:133]
	v_lshl_add_u64 v[66:67], v[222:223], 0, v[66:67]
	global_load_dwordx4 v[124:127], v[66:67], off nt
	global_load_dwordx4 v[128:131], v[66:67], off offset:64 nt
	global_load_dwordx4 v[136:139], v[66:67], off offset:512 nt
	global_load_dwordx4 v[140:143], v[66:67], off offset:576 nt
	global_load_dword v122, v[226:227], off offset:576
	v_lshlrev_b64 v[66:67], 13, v[146:147]
	v_lshl_add_u64 v[66:67], v[222:223], 0, v[66:67]
	global_load_dwordx4 v[110:113], v[66:67], off nt
	global_load_dwordx4 v[106:109], v[66:67], off offset:64 nt
	global_load_dwordx4 v[102:105], v[66:67], off offset:512 nt
	global_load_dwordx4 v[98:101], v[66:67], off offset:576 nt
	global_load_dword v118, v[226:227], off offset:640
	v_lshlrev_b64 v[66:67], 13, v[120:121]
	v_lshl_add_u64 v[66:67], v[222:223], 0, v[66:67]
	global_load_dwordx4 v[94:97], v[66:67], off nt
	global_load_dwordx4 v[90:93], v[66:67], off offset:64 nt
	global_load_dwordx4 v[86:89], v[66:67], off offset:512 nt
	global_load_dwordx4 v[82:85], v[66:67], off offset:576 nt
	global_load_dword v114, v[226:227], off offset:704
	v_lshlrev_b64 v[66:67], 13, v[116:117]
	v_lshl_add_u64 v[66:67], v[222:223], 0, v[66:67]
	global_load_dwordx4 v[78:81], v[66:67], off nt
	global_load_dwordx4 v[74:77], v[66:67], off offset:64 nt
	global_load_dwordx4 v[70:73], v[66:67], off offset:512 nt
	s_nop 0
	global_load_dwordx4 v[66:69], v[66:67], off offset:576 nt
	v_lshlrev_b64 v[132:133], 12, v[132:133]
	s_waitcnt vmcnt(19)
	v_pk_mul_f32 v[148:149], v[218:219], v[144:145] op_sel_hi:[1,0]
	v_pk_mul_f32 v[150:151], v[220:221], v[144:145] op_sel_hi:[1,0]
	s_waitcnt vmcnt(18)
	v_pk_fma_f32 v[64:65], v[148:149], v[64:65], v[126:127]
	v_pk_fma_f32 v[62:63], v[150:151], v[62:63], v[124:125]
	v_pk_mul_f32 v[124:125], v[216:217], v[144:145] op_sel_hi:[1,0]
	v_cvt_pk_bf16_f32 v62, v62, v63
	v_cvt_pk_bf16_f32 v63, v64, v65
	v_lshl_add_u64 v[64:65], s[8:9], 0, v[132:133]
	v_lshl_add_u64 v[64:65], v[64:65], 0, v[134:135]
	global_store_dwordx2 v[64:65], v[62:63], off
	v_pk_mul_f32 v[62:63], v[214:215], v[144:145] op_sel_hi:[1,0]
	s_waitcnt vmcnt(18)
	v_pk_fma_f32 v[58:59], v[124:125], v[58:59], v[128:129]
	v_pk_fma_f32 v[60:61], v[62:63], v[60:61], v[130:131]
	v_cvt_pk_bf16_f32 v58, v58, v59
	s_nop 0
	v_cvt_pk_bf16_f32 v59, v60, v61
	v_pk_mul_f32 v[60:61], v[212:213], v[144:145] op_sel_hi:[1,0]
	global_store_dwordx2 v[64:65], v[58:59], off offset:32
	v_pk_mul_f32 v[58:59], v[210:211], v[144:145] op_sel_hi:[1,0]
	s_waitcnt vmcnt(18)
	v_pk_fma_f32 v[54:55], v[60:61], v[54:55], v[136:137]
	v_pk_fma_f32 v[56:57], v[58:59], v[56:57], v[138:139]
	v_cvt_pk_bf16_f32 v54, v54, v55
	s_nop 0
	v_cvt_pk_bf16_f32 v55, v56, v57
	global_store_dwordx2 v[64:65], v[54:55], off offset:256
	v_pk_mul_f32 v[54:55], v[206:207], v[144:145] op_sel_hi:[1,0]
	v_pk_mul_f32 v[56:57], v[208:209], v[144:145] op_sel_hi:[1,0]
	s_waitcnt vmcnt(18)
	v_pk_fma_f32 v[52:53], v[54:55], v[52:53], v[142:143]
	v_pk_fma_f32 v[50:51], v[56:57], v[50:51], v[140:141]
	s_waitcnt vmcnt(17)
	v_pk_mul_f32 v[54:55], v[220:221], v[122:123] op_sel_hi:[1,0]
	v_cvt_pk_bf16_f32 v50, v50, v51
	v_cvt_pk_bf16_f32 v51, v52, v53
	v_pk_mul_f32 v[52:53], v[218:219], v[122:123] op_sel_hi:[1,0]
	global_store_dwordx2 v[64:65], v[50:51], off offset:288
	v_lshlrev_b64 v[50:51], 12, v[146:147]
	s_waitcnt vmcnt(17)
	v_pk_fma_f32 v[48:49], v[52:53], v[48:49], v[112:113]
	v_pk_fma_f32 v[46:47], v[54:55], v[46:47], v[110:111]
	s_nop 0
	v_cvt_pk_bf16_f32 v46, v46, v47
	v_cvt_pk_bf16_f32 v47, v48, v49
	v_lshl_add_u64 v[48:49], s[8:9], 0, v[50:51]
	v_lshl_add_u64 v[48:49], v[48:49], 0, v[134:135]
	global_store_dwordx2 v[48:49], v[46:47], off
	v_pk_mul_f32 v[46:47], v[214:215], v[122:123] op_sel_hi:[1,0]
	v_pk_mul_f32 v[50:51], v[216:217], v[122:123] op_sel_hi:[1,0]
	s_waitcnt vmcnt(17)
	v_pk_fma_f32 v[44:45], v[46:47], v[44:45], v[108:109]
	v_pk_fma_f32 v[42:43], v[50:51], v[42:43], v[106:107]
	s_nop 0
	v_cvt_pk_bf16_f32 v42, v42, v43
	v_cvt_pk_bf16_f32 v43, v44, v45
	v_pk_mul_f32 v[44:45], v[212:213], v[122:123] op_sel_hi:[1,0]
	global_store_dwordx2 v[48:49], v[42:43], off offset:32
	v_pk_mul_f32 v[42:43], v[210:211], v[122:123] op_sel_hi:[1,0]
	s_waitcnt vmcnt(17)
	v_pk_fma_f32 v[38:39], v[44:45], v[38:39], v[102:103]
	v_pk_fma_f32 v[40:41], v[42:43], v[40:41], v[104:105]
	v_cvt_pk_bf16_f32 v38, v38, v39
	s_nop 0
	v_cvt_pk_bf16_f32 v39, v40, v41
	global_store_dwordx2 v[48:49], v[38:39], off offset:256
	v_pk_mul_f32 v[38:39], v[206:207], v[122:123] op_sel_hi:[1,0]
	v_pk_mul_f32 v[40:41], v[208:209], v[122:123] op_sel_hi:[1,0]
	s_waitcnt vmcnt(17)
	v_pk_fma_f32 v[36:37], v[38:39], v[36:37], v[100:101]
	v_pk_fma_f32 v[34:35], v[40:41], v[34:35], v[98:99]
	s_waitcnt vmcnt(16)
	v_pk_mul_f32 v[38:39], v[220:221], v[118:119] op_sel_hi:[1,0]
	v_cvt_pk_bf16_f32 v34, v34, v35
	v_cvt_pk_bf16_f32 v35, v36, v37
	v_pk_mul_f32 v[36:37], v[218:219], v[118:119] op_sel_hi:[1,0]
	global_store_dwordx2 v[48:49], v[34:35], off offset:288
	v_lshlrev_b64 v[34:35], 12, v[120:121]
	s_waitcnt vmcnt(16)
	v_pk_fma_f32 v[32:33], v[36:37], v[32:33], v[96:97]
	v_pk_fma_f32 v[30:31], v[38:39], v[30:31], v[94:95]
	s_nop 0
	v_cvt_pk_bf16_f32 v30, v30, v31
	v_cvt_pk_bf16_f32 v31, v32, v33
	v_lshl_add_u64 v[32:33], s[8:9], 0, v[34:35]
	v_lshl_add_u64 v[32:33], v[32:33], 0, v[134:135]
	global_store_dwordx2 v[32:33], v[30:31], off
	v_pk_mul_f32 v[30:31], v[214:215], v[118:119] op_sel_hi:[1,0]
	v_pk_mul_f32 v[34:35], v[216:217], v[118:119] op_sel_hi:[1,0]
	s_waitcnt vmcnt(16)
	v_pk_fma_f32 v[24:25], v[30:31], v[24:25], v[92:93]
	v_pk_fma_f32 v[22:23], v[34:35], v[22:23], v[90:91]
	s_nop 0
	v_cvt_pk_bf16_f32 v22, v22, v23
	v_cvt_pk_bf16_f32 v23, v24, v25
	v_pk_mul_f32 v[24:25], v[212:213], v[118:119] op_sel_hi:[1,0]
	global_store_dwordx2 v[32:33], v[22:23], off offset:32
	v_pk_mul_f32 v[22:23], v[210:211], v[118:119] op_sel_hi:[1,0]
	s_waitcnt vmcnt(16)
	v_pk_fma_f32 v[24:25], v[24:25], v[26:27], v[86:87]
	v_pk_fma_f32 v[22:23], v[22:23], v[28:29], v[88:89]
	v_cvt_pk_bf16_f32 v24, v24, v25
	s_nop 0
	v_cvt_pk_bf16_f32 v25, v22, v23
	global_store_dwordx2 v[32:33], v[24:25], off offset:256
	v_pk_mul_f32 v[22:23], v[206:207], v[118:119] op_sel_hi:[1,0]
	v_pk_mul_f32 v[24:25], v[208:209], v[118:119] op_sel_hi:[1,0]
	s_waitcnt vmcnt(16)
	v_pk_fma_f32 v[20:21], v[22:23], v[20:21], v[84:85]
	v_pk_fma_f32 v[18:19], v[24:25], v[18:19], v[82:83]
	s_waitcnt vmcnt(15)
	v_pk_mul_f32 v[22:23], v[220:221], v[114:115] op_sel_hi:[1,0]
	v_cvt_pk_bf16_f32 v18, v18, v19
	v_cvt_pk_bf16_f32 v19, v20, v21
	v_pk_mul_f32 v[20:21], v[218:219], v[114:115] op_sel_hi:[1,0]
	global_store_dwordx2 v[32:33], v[18:19], off offset:288
	v_lshlrev_b64 v[18:19], 12, v[116:117]
	s_waitcnt vmcnt(15)
	v_pk_fma_f32 v[12:13], v[20:21], v[12:13], v[80:81]
	v_pk_fma_f32 v[10:11], v[22:23], v[10:11], v[78:79]
	s_nop 0
	v_cvt_pk_bf16_f32 v10, v10, v11
	v_cvt_pk_bf16_f32 v11, v12, v13
	v_lshl_add_u64 v[12:13], s[8:9], 0, v[18:19]
	v_lshl_add_u64 v[12:13], v[12:13], 0, v[134:135]
	global_store_dwordx2 v[12:13], v[10:11], off
	v_pk_mul_f32 v[10:11], v[214:215], v[114:115] op_sel_hi:[1,0]
	v_pk_mul_f32 v[18:19], v[216:217], v[114:115] op_sel_hi:[1,0]
	s_waitcnt vmcnt(15)
	v_pk_fma_f32 v[4:5], v[10:11], v[4:5], v[76:77]
	v_cvt_f32_i32_e32 v11, v15
	v_cvt_f32_i32_e32 v10, v14
	v_cvt_f32_i32_e32 v15, v17
	v_cvt_f32_i32_e32 v14, v16
	v_pk_fma_f32 v[2:3], v[18:19], v[2:3], v[74:75]
	s_nop 0
	v_cvt_pk_bf16_f32 v2, v2, v3
	v_cvt_pk_bf16_f32 v3, v4, v5
	v_pk_mul_f32 v[4:5], v[212:213], v[114:115] op_sel_hi:[1,0]
	global_store_dwordx2 v[12:13], v[2:3], off offset:32
	v_pk_mul_f32 v[2:3], v[210:211], v[114:115] op_sel_hi:[1,0]
	s_waitcnt vmcnt(15)
	v_pk_fma_f32 v[4:5], v[4:5], v[10:11], v[70:71]
	v_pk_fma_f32 v[2:3], v[2:3], v[14:15], v[72:73]
	v_cvt_pk_bf16_f32 v4, v4, v5
	s_nop 0
	v_cvt_pk_bf16_f32 v5, v2, v3
	global_store_dwordx2 v[12:13], v[4:5], off offset:256
	v_pk_mul_f32 v[4:5], v[208:209], v[114:115] op_sel_hi:[1,0]
	v_pk_mul_f32 v[2:3], v[206:207], v[114:115] op_sel_hi:[1,0]
	s_waitcnt vmcnt(15)
	v_pk_fma_f32 v[4:5], v[4:5], v[6:7], v[66:67]
	v_pk_fma_f32 v[2:3], v[2:3], v[8:9], v[68:69]
	v_cvt_pk_bf16_f32 v4, v4, v5
	s_nop 0
	v_cvt_pk_bf16_f32 v5, v2, v3
	global_store_dwordx2 v[12:13], v[4:5], off offset:288
	s_cbranch_vccnz .LBB0_603
	s_andn2_b64 vcc, exec, s[0:1]
	s_cbranch_vccnz .LBB0_602
	s_barrier
	s_branch .LBB0_602
